# P1 conversion stream: a wave that has seen the stop flag skips the pipelined reload of its current item (16 dead loads) before winding down
# speedup vs baseline: 1.0090x; 1.0058x over previous
; __device__ __forceinline__ void t128_load(const float* W, int N, int item, int lane, f32x4 (&v)[16]) {
;     const int nblk = N / 32, kb = item / nblk, nb = item % nblk, k0 = 128 * kb, n0 = 32 * nb;
; #pragma unroll
;     for (int i = 0; i < 16; ++i) v[i] = __builtin_nontemporal_load((const f32x4*)(W + (size_t)(k0 + i * 8 + (lane >> 3)) * N + n0 + (lane & 7) * 4));
; }
; __device__ __forceinline__ void cs_load(int it, int lane, const float* w_gu, const float* w_d, f32x4 (&v)[16]) {
;     if (it < I_D) { constexpr int per = (DFF / 128) * (D / 32); t128_load(w_d + (size_t)(it / per) * DFF * D, D, it % per, lane, v); }
;     else { const int r = it - I_D; constexpr int per = (D / 128) * (4096 / 32); t128_load(w_gu + (size_t)(r / per) * D * 4096, 4096, r % per, lane, v); }
; }
; __device__ __forceinline__ void cs_store(const Ctx& c, int it, const f32x4 (&v)[16], unsigned char* Wgu, unsigned char* Wd) {
;     if (it < I_D) { constexpr int per = (DFF / 128) * (D / 32); t128_store<0>(c, v, DFF, D, Wd + (size_t)(it / per) * D * DFF, it % per); }
;     else { const int r = it - I_D; constexpr int per = (D / 128) * (4096 / 32); t128_store<1>(c, v, D, 4096, Wgu + (size_t)(r / per) * 4096 * D, r % per); }
; }
; __device__ __forceinline__ int conv_stream(const Ctx& c, int j, int first, int step, const unsigned* stop, const float* w_gu, const float* w_d, unsigned char* Wgu, unsigned char* Wd) {
;     int i = first;
;     if (j + CONV_SLOTS * i >= CONV_TOTAL) return i;
;     if (stop && stop_poll(c, stop) >= STOP_AT) return i;
;     f32x4 va[16], vb[16];
;     cs_load(j + CONV_SLOTS * i, c.lane, w_gu, w_d, va);
;     for (;;) {
;         { const int i2 = i + step; const bool more = j + CONV_SLOTS * i2 < CONV_TOTAL && !(stop && stop_poll(c, stop) >= STOP_AT);
;           cs_load(j + CONV_SLOTS * (more ? i2 : i), c.lane, w_gu, w_d, vb);
;           cs_store(c, j + CONV_SLOTS * i, va, Wgu, Wd); i = i2; if (!more) break; }
;         { const int i2 = i + step; const bool more = j + CONV_SLOTS * i2 < CONV_TOTAL && !(stop && stop_poll(c, stop) >= STOP_AT);
;           cs_load(j + CONV_SLOTS * (more ? i2 : i), c.lane, w_gu, w_d, va);
;           cs_store(c, j + CONV_SLOTS * i, vb, Wgu, Wd); i = i2; if (!more) break; }
.LBB0_271:
	s_waitcnt vmcnt(4)
	v_or_b32_e32 v122, s21, v131
	v_ashrrev_i32_e32 v123, 31, v122
	v_lshlrev_b64 v[66:67], s46, v[122:123]
	v_add_u32_e32 v68, 8, v122
	v_add_u32_e32 v74, 16, v122
	v_add_u32_e32 v76, 24, v122
	v_add_u32_e32 v82, 32, v122
	v_add_u32_e32 v84, 40, v122
	v_add_u32_e32 v90, 48, v122
	v_add_u32_e32 v92, 56, v122
	v_add_u32_e32 v98, 64, v122
	v_add_u32_e32 v100, 0x48, v122
	v_add_u32_e32 v106, 0x50, v122
	v_add_u32_e32 v108, 0x58, v122
	v_add_u32_e32 v114, 0x60, v122
	v_add_u32_e32 v116, 0x68, v122
	v_add_u32_e32 v126, 0x70, v122
	v_add_u32_e32 v122, 0x78, v122
	v_lshlrev_b32_e32 v132, 2, v130
	v_ashrrev_i32_e32 v69, 31, v68
	v_ashrrev_i32_e32 v75, 31, v74
	v_ashrrev_i32_e32 v77, 31, v76
	v_ashrrev_i32_e32 v83, 31, v82
	v_ashrrev_i32_e32 v85, 31, v84
	v_ashrrev_i32_e32 v91, 31, v90
	v_ashrrev_i32_e32 v93, 31, v92
	v_ashrrev_i32_e32 v99, 31, v98
	v_ashrrev_i32_e32 v101, 31, v100
	v_ashrrev_i32_e32 v107, 31, v106
	v_ashrrev_i32_e32 v109, 31, v108
	v_ashrrev_i32_e32 v115, 31, v114
	v_ashrrev_i32_e32 v117, 31, v116
	v_ashrrev_i32_e32 v127, 31, v126
	v_ashrrev_i32_e32 v123, 31, v122
	v_lshl_add_u64 v[124:125], s[48:49], 0, v[132:133]
	v_lshlrev_b64 v[68:69], s46, v[68:69]
	v_lshlrev_b64 v[74:75], s46, v[74:75]
	v_lshlrev_b64 v[76:77], s46, v[76:77]
	v_lshlrev_b64 v[82:83], s46, v[82:83]
	v_lshlrev_b64 v[84:85], s46, v[84:85]
	v_lshlrev_b64 v[90:91], s46, v[90:91]
	v_lshlrev_b64 v[92:93], s46, v[92:93]
	v_lshlrev_b64 v[98:99], s46, v[98:99]
	v_lshlrev_b64 v[100:101], s46, v[100:101]
	v_lshlrev_b64 v[106:107], s46, v[106:107]
	v_lshlrev_b64 v[108:109], s46, v[108:109]
	v_lshlrev_b64 v[114:115], s46, v[114:115]
	v_lshlrev_b64 v[116:117], s46, v[116:117]
	v_lshlrev_b64 v[126:127], s46, v[126:127]
	v_lshlrev_b64 v[122:123], s46, v[122:123]
	v_lshl_add_u64 v[66:67], v[124:125], 0, v[66:67]
	v_lshl_add_u64 v[68:69], v[124:125], 0, v[68:69]
	v_lshl_add_u64 v[74:75], v[124:125], 0, v[74:75]
	v_lshl_add_u64 v[76:77], v[124:125], 0, v[76:77]
	v_lshl_add_u64 v[82:83], v[124:125], 0, v[82:83]
	v_lshl_add_u64 v[84:85], v[124:125], 0, v[84:85]
	v_lshl_add_u64 v[90:91], v[124:125], 0, v[90:91]
	v_lshl_add_u64 v[92:93], v[124:125], 0, v[92:93]
	v_lshl_add_u64 v[98:99], v[124:125], 0, v[98:99]
	v_lshl_add_u64 v[100:101], v[124:125], 0, v[100:101]
	v_lshl_add_u64 v[106:107], v[124:125], 0, v[106:107]
	v_lshl_add_u64 v[108:109], v[124:125], 0, v[108:109]
	v_lshl_add_u64 v[114:115], v[124:125], 0, v[114:115]
	v_lshl_add_u64 v[116:117], v[124:125], 0, v[116:117]
	v_lshl_add_u64 v[126:127], v[124:125], 0, v[126:127]
	v_lshl_add_u64 v[122:123], v[124:125], 0, v[122:123]
	s_and_b64 vcc, exec, s[44:45]
	s_cbranch_vccz .Lcv1a_noload
	global_load_dwordx4 v[70:73], v[66:67], off nt
	s_nop 0
	global_load_dwordx4 v[66:69], v[68:69], off nt
	s_nop 0
	global_load_dwordx4 v[78:81], v[74:75], off nt
	s_nop 0
	global_load_dwordx4 v[74:77], v[76:77], off nt
	s_nop 0
	global_load_dwordx4 v[86:89], v[82:83], off nt
	s_nop 0
	global_load_dwordx4 v[82:85], v[84:85], off nt
	s_nop 0
	global_load_dwordx4 v[94:97], v[90:91], off nt
	s_nop 0
	global_load_dwordx4 v[90:93], v[92:93], off nt
	s_nop 0
	global_load_dwordx4 v[102:105], v[98:99], off nt
	s_nop 0
	global_load_dwordx4 v[98:101], v[100:101], off nt
	s_nop 0
	global_load_dwordx4 v[110:113], v[106:107], off nt
	s_nop 0
	global_load_dwordx4 v[106:109], v[108:109], off nt
	s_nop 0
	global_load_dwordx4 v[118:121], v[114:115], off nt
	s_nop 0
	global_load_dwordx4 v[114:117], v[116:117], off nt
	s_nop 0
	global_load_dwordx4 v[126:129], v[126:127], off nt
	s_nop 0
	global_load_dwordx4 v[122:125], v[122:123], off nt
.Lcv1a_noload:
	s_add_i32 s26, s19, 0xfffff800
	s_mov_b64 s[46:47], -1
	s_cmpk_gt_i32 s26, 0x7fff
	v_add_u32_e32 v156, 0x1080, v146
	v_add_u32_e32 v157, 0x1088, v146
	v_add_u32_e32 v158, 0x14a0, v146
	v_add_u32_e32 v159, 0x14a8, v146
	v_add_u32_e32 v160, 0x18c0, v146
	v_add_u32_e32 v161, 0x18c8, v146
	v_add_u32_e32 v162, 0x1ce0, v146
	v_add_u32_e32 v163, 0x1ce8, v146
	v_add_u32_e32 v164, 0x2100, v146
	v_add_u32_e32 v165, 0x2108, v146
	v_add_u32_e32 v166, 0x2520, v146
	v_add_u32_e32 v167, 0x2528, v146
	v_add_u32_e32 v168, 0x2940, v146
	v_add_u32_e32 v169, 0x2948, v146
	v_add_u32_e32 v170, 0x2d60, v146
	v_add_u32_e32 v171, 0x2d68, v146
	v_add_u32_e32 v172, 0x3180, v146
	v_add_u32_e32 v173, 0x3188, v146
	v_add_u32_e32 v174, 0x35a0, v146
	v_add_u32_e32 v175, 0x35a8, v146
	v_add_u32_e32 v176, 0x39c0, v146
	v_add_u32_e32 v177, 0x39c8, v146
	v_add_u32_e32 v178, 0x3de0, v146
	v_add_u32_e32 v179, 0x3de8, v146
	v_add_u32_e32 v155, 0x400, v150
	v_add_u32_e32 v154, 0x600, v150
	s_cbranch_scc0 .LBB0_290
; #define LAS __attribute__((address_space(3)))
; #define LDS_WAIT() asm volatile("s_waitcnt lgkmcnt(0)" ::: "memory")
; template <int MODE>
; __device__ __forceinline__ void t128_store(const Ctx& c, const f32x4 (&v)[16], int K, int N, unsigned char* WT, int item) {
;     LAS float* scr = (LAS float*)(c.lds + c.wave * CONV_SCR);
;     const int nblk = N / 32, kb = item / nblk, nb = item % nblk, k0 = 128 * kb, n0 = 32 * nb, lane = c.lane;
; #pragma unroll
;     for (int i = 0; i < 16; ++i) { LAS float* d = scr + (i * 8 + (lane >> 3)) * 33 + (lane & 7) * 4; d[0] = v[i].x; d[1] = v[i].y; d[2] = v[i].z; d[3] = v[i].w; }
;     LDS_WAIT(); asm volatile("" ::: "memory");
;     const int cc = lane & 7;
; #pragma unroll
;     for (int j = 0; j < 4; ++j) { const int n = (lane >> 3) + 8 * j; const LAS float* s = scr + (16 * cc) * 33 + n; int w[4];
; #pragma unroll
;         for (int q = 0; q < 4; ++q) { int t = 0; t = __builtin_amdgcn_cvt_pk_fp8_f32(s[(4 * q) * 33] * WSCALE, s[(4 * q + 1) * 33] * WSCALE, t, false);
;             t = __builtin_amdgcn_cvt_pk_fp8_f32(s[(4 * q + 2) * 33] * WSCALE, s[(4 * q + 3) * 33] * WSCALE, t, true); w[q] = t; }
;         const int dr = drow_of<MODE>(n0 + n);
;         __builtin_nontemporal_store((u32x4){(unsigned)w[0], (unsigned)w[1], (unsigned)w[2], (unsigned)w[3]}, (u32x4*)(WT + (size_t)dr * K + k0 + 16 * cc)); }
;     LDS_WAIT(); asm volatile("" ::: "memory");
; }
; __device__ __forceinline__ void cs_store(const Ctx& c, int it, const f32x4 (&v)[16], unsigned char* Wgu, unsigned char* Wd) {
;     if (it < I_D) { constexpr int per = (DFF / 128) * (D / 32); t128_store<0>(c, v, DFF, D, Wd + (size_t)(it / per) * D * DFF, it % per); }
;     else { const int r = it - I_D; constexpr int per = (D / 128) * (4096 / 32); t128_store<1>(c, v, D, 4096, Wgu + (size_t)(r / per) * 4096 * D, r % per); }
	s_nop 0
	ds_write2_b32 v146, v6, v7 offset1:1
	ds_write2_b32 v146, v8, v9 offset0:2 offset1:3
	ds_write2_b32 v151, v2, v3 offset1:1
	ds_write2_b32 v151, v4, v5 offset0:2 offset1:3
	ds_write2_b32 v152, v14, v15 offset1:1
	ds_write2_b32 v152, v16, v17 offset0:2 offset1:3
	ds_write2_b32 v153, v10, v11 offset1:1
	ds_write2_b32 v153, v12, v13 offset0:2 offset1:3
	ds_write2_b32 v156, v22, v23 offset1:1
	ds_write2_b32 v157, v24, v25 offset1:1
	ds_write2_b32 v158, v18, v19 offset1:1
	ds_write2_b32 v159, v20, v21 offset1:1
	ds_write2_b32 v160, v30, v31 offset1:1
	ds_write2_b32 v161, v32, v33 offset1:1
	ds_write2_b32 v162, v26, v27 offset1:1
	ds_write2_b32 v163, v28, v29 offset1:1
	ds_write2_b32 v164, v38, v39 offset1:1
	ds_write2_b32 v165, v40, v41 offset1:1
	ds_write2_b32 v166, v34, v35 offset1:1
	ds_write2_b32 v167, v36, v37 offset1:1
	ds_write2_b32 v168, v46, v47 offset1:1
	ds_write2_b32 v169, v48, v49 offset1:1
	ds_write2_b32 v170, v42, v43 offset1:1
	ds_write2_b32 v171, v44, v45 offset1:1
	ds_write2_b32 v172, v54, v55 offset1:1
	ds_write2_b32 v173, v56, v57 offset1:1
	ds_write2_b32 v174, v50, v51 offset1:1
	ds_write2_b32 v175, v52, v53 offset1:1
	ds_write2_b32 v176, v62, v63 offset1:1
	ds_write2_b32 v177, v64, v65 offset1:1
	ds_write2_b32 v178, v58, v59 offset1:1
	ds_write2_b32 v179, v60, v61 offset1:1
	s_waitcnt lgkmcnt(0)
	ds_read2_b32 v[184:185], v150 offset1:8
	ds_read2_b32 v[186:187], v150 offset0:33 offset1:41
	ds_read2_b32 v[190:191], v150 offset0:66 offset1:74
	ds_read2_b32 v[192:193], v150 offset0:99 offset1:107
	v_mov_b32_e32 v180, v133
	ds_read2_b32 v[194:195], v150 offset0:132 offset1:140
	ds_read2_b32 v[196:197], v150 offset0:165 offset1:173
	s_waitcnt lgkmcnt(5)
	v_mul_f32_e32 v181, 0x42800000, v184
	s_waitcnt lgkmcnt(4)
	v_mul_f32_e32 v182, 0x42800000, v186
	v_cvt_pk_fp8_f32 v180, v181, v182
	s_waitcnt lgkmcnt(3)
	v_mul_f32_e32 v181, 0x42800000, v190
	s_waitcnt lgkmcnt(2)
	v_mul_f32_e32 v182, 0x42800000, v192
	ds_read2_b32 v[198:199], v150 offset0:198 offset1:206
	ds_read2_b32 v[200:201], v150 offset0:231 offset1:239
	v_cvt_pk_fp8_f32 v180, v181, v182 op_sel:[0,0,1]
	s_waitcnt lgkmcnt(3)
	v_mul_f32_e32 v182, 0x42800000, v194
	s_waitcnt lgkmcnt(2)
	v_mul_f32_e32 v183, 0x42800000, v196
	v_mov_b32_e32 v181, v133
	ds_read2_b32 v[202:203], v155 offset0:8 offset1:16
	ds_read2_b32 v[204:205], v155 offset0:41 offset1:49
	v_cvt_pk_fp8_f32 v181, v182, v183
	ds_read2_b32 v[206:207], v155 offset0:74 offset1:82
	ds_read2_b32 v[208:209], v155 offset0:107 offset1:115
	ds_read2_b32 v[210:211], v155 offset0:140 offset1:148
	ds_read2_b32 v[212:213], v155 offset0:173 offset1:181
	s_waitcnt lgkmcnt(7)
	v_mul_f32_e32 v182, 0x42800000, v198
	s_waitcnt lgkmcnt(6)
	v_mul_f32_e32 v183, 0x42800000, v200
	v_cvt_pk_fp8_f32 v181, v182, v183 op_sel:[0,0,1]
	s_waitcnt lgkmcnt(5)
	v_mul_f32_e32 v183, 0x42800000, v202
	s_waitcnt lgkmcnt(4)
	v_mul_f32_e32 v184, 0x42800000, v204
	v_mov_b32_e32 v182, v133
	ds_read2_b32 v[214:215], v155 offset0:206 offset1:214
	ds_read2_b32 v[216:217], v155 offset0:239 offset1:247
	v_cvt_pk_fp8_f32 v182, v183, v184
	s_waitcnt lgkmcnt(3)
	v_mul_f32_e32 v190, 0x42800000, v210
	s_waitcnt lgkmcnt(2)
	v_mul_f32_e32 v192, 0x42800000, v212
	v_mov_b32_e32 v183, v133
	v_cvt_pk_fp8_f32 v183, v190, v192
	v_mul_f32_e32 v184, 0x42800000, v206
	v_mul_f32_e32 v186, 0x42800000, v208
	v_cvt_pk_fp8_f32 v182, v184, v186 op_sel:[0,0,1]
	s_waitcnt lgkmcnt(1)
	v_mul_f32_e32 v184, 0x42800000, v214
	s_waitcnt lgkmcnt(0)
; #define LAS __attribute__((address_space(3)))
; #define LDS_WAIT() asm volatile("s_waitcnt lgkmcnt(0)" ::: "memory")
; template <int MODE>
; __device__ __forceinline__ void t128_store(const Ctx& c, const f32x4 (&v)[16], int K, int N, unsigned char* WT, int item) {
;     LAS float* scr = (LAS float*)(c.lds + c.wave * CONV_SCR);
;     const int nblk = N / 32, kb = item / nblk, nb = item % nblk, k0 = 128 * kb, n0 = 32 * nb, lane = c.lane;
; #pragma unroll
;     for (int i = 0; i < 16; ++i) { LAS float* d = scr + (i * 8 + (lane >> 3)) * 33 + (lane & 7) * 4; d[0] = v[i].x; d[1] = v[i].y; d[2] = v[i].z; d[3] = v[i].w; }
;     LDS_WAIT(); asm volatile("" ::: "memory");
;     const int cc = lane & 7;
; #pragma unroll
;     for (int j = 0; j < 4; ++j) { const int n = (lane >> 3) + 8 * j; const LAS float* s = scr + (16 * cc) * 33 + n; int w[4];
; #pragma unroll
;         for (int q = 0; q < 4; ++q) { int t = 0; t = __builtin_amdgcn_cvt_pk_fp8_f32(s[(4 * q) * 33] * WSCALE, s[(4 * q + 1) * 33] * WSCALE, t, false);
;             t = __builtin_amdgcn_cvt_pk_fp8_f32(s[(4 * q + 2) * 33] * WSCALE, s[(4 * q + 3) * 33] * WSCALE, t, true); w[q] = t; }
;         const int dr = drow_of<MODE>(n0 + n);
;         __builtin_nontemporal_store((u32x4){(unsigned)w[0], (unsigned)w[1], (unsigned)w[2], (unsigned)w[3]}, (u32x4*)(WT + (size_t)dr * K + k0 + 16 * cc)); }
;     LDS_WAIT(); asm volatile("" ::: "memory");
; }
; __device__ __forceinline__ void cs_store(const Ctx& c, int it, const f32x4 (&v)[16], unsigned char* Wgu, unsigned char* Wd) {
;     if (it < I_D) { constexpr int per = (DFF / 128) * (D / 32); t128_store<0>(c, v, DFF, D, Wd + (size_t)(it / per) * D * DFF, it % per); }
;     else { const int r = it - I_D; constexpr int per = (D / 128) * (4096 / 32); t128_store<1>(c, v, D, 4096, Wgu + (size_t)(r / per) * 4096 * D, r % per); }
	v_mul_f32_e32 v186, 0x42800000, v216
	v_cvt_pk_fp8_f32 v183, v184, v186 op_sel:[0,0,1]
	v_mul_f32_e32 v185, 0x42800000, v185
	v_mul_f32_e32 v186, 0x42800000, v187
	v_mov_b32_e32 v184, v133
	v_cvt_pk_fp8_f32 v184, v185, v186
	v_mul_f32_e32 v186, 0x42800000, v191
	v_mul_f32_e32 v190, 0x42800000, v195
	v_mul_f32_e32 v191, 0x42800000, v197
	v_mov_b32_e32 v185, v133
	v_cvt_pk_fp8_f32 v185, v190, v191
	v_mul_f32_e32 v187, 0x42800000, v193
	v_cvt_pk_fp8_f32 v184, v186, v187 op_sel:[0,0,1]
	v_mul_f32_e32 v186, 0x42800000, v199
	v_mul_f32_e32 v187, 0x42800000, v201
	v_cvt_pk_fp8_f32 v185, v186, v187 op_sel:[0,0,1]
	v_mul_f32_e32 v187, 0x42800000, v203
	v_mul_f32_e32 v190, 0x42800000, v205
	v_mov_b32_e32 v186, v133
	v_cvt_pk_fp8_f32 v186, v187, v190
	v_mul_f32_e32 v192, 0x42800000, v211
	v_mul_f32_e32 v193, 0x42800000, v213
	v_mov_b32_e32 v187, v133
	v_cvt_pk_fp8_f32 v187, v192, v193
	s_add_i32 s20, s19, 0xffff7800
	v_mul_f32_e32 v190, 0x42800000, v207
	v_mul_f32_e32 v191, 0x42800000, v209
	s_lshr_b32 s42, s20, 11
	v_cvt_pk_fp8_f32 v186, v190, v191 op_sel:[0,0,1]
	v_mul_f32_e32 v190, 0x42800000, v215
	v_mul_f32_e32 v191, 0x42800000, v217
	s_lshl_b64 s[20:21], s[42:43], 23
	v_cvt_pk_fp8_f32 v187, v190, v191 op_sel:[0,0,1]
	v_lshl_add_u64 v[188:189], v[136:137], 0, s[20:21]
	ds_read2_b32 v[190:191], v150 offset0:16 offset1:24
	ds_read2_b32 v[192:193], v150 offset0:49 offset1:57
	v_lshl_add_u64 v[218:219], v[188:189], 0, v[138:139]
	global_store_dwordx4 v[218:219], v[180:183], off nt
	s_nop 1
	v_lshl_add_u64 v[180:181], v[188:189], 0, v[140:141]
	global_store_dwordx4 v[180:181], v[184:187], off nt
	ds_read2_b32 v[184:185], v150 offset0:82 offset1:90
	ds_read2_b32 v[186:187], v150 offset0:115 offset1:123
	s_waitcnt lgkmcnt(3)
	v_mul_f32_e32 v181, 0x42800000, v190
	s_waitcnt lgkmcnt(2)
	v_mul_f32_e32 v182, 0x42800000, v192
	v_mov_b32_e32 v180, v133
	ds_read2_b32 v[194:195], v150 offset0:148 offset1:156
	ds_read2_b32 v[196:197], v150 offset0:181 offset1:189
	v_cvt_pk_fp8_f32 v180, v181, v182
	s_waitcnt lgkmcnt(3)
	v_mul_f32_e32 v181, 0x42800000, v184
	s_waitcnt lgkmcnt(2)
	v_mul_f32_e32 v182, 0x42800000, v186
	ds_read2_b32 v[198:199], v150 offset0:214 offset1:222
	ds_read2_b32 v[200:201], v150 offset0:247 offset1:255
	v_cvt_pk_fp8_f32 v180, v181, v182 op_sel:[0,0,1]
	s_waitcnt lgkmcnt(3)
	v_mul_f32_e32 v182, 0x42800000, v194
	s_waitcnt lgkmcnt(2)
	v_mul_f32_e32 v183, 0x42800000, v196
	v_mov_b32_e32 v181, v133
	ds_read2_b32 v[202:203], v155 offset0:24 offset1:32
	ds_read2_b32 v[204:205], v155 offset0:57 offset1:65
	v_cvt_pk_fp8_f32 v181, v182, v183
	ds_read2_b32 v[206:207], v155 offset0:90 offset1:98
	ds_read2_b32 v[208:209], v155 offset0:123 offset1:131
	ds_read2_b32 v[210:211], v155 offset0:156 offset1:164
	ds_read2_b32 v[212:213], v155 offset0:189 offset1:197
	s_waitcnt lgkmcnt(7)
	v_mul_f32_e32 v182, 0x42800000, v198
	s_waitcnt lgkmcnt(6)
	v_mul_f32_e32 v183, 0x42800000, v200
	v_cvt_pk_fp8_f32 v181, v182, v183 op_sel:[0,0,1]
	s_waitcnt lgkmcnt(5)
	v_mul_f32_e32 v183, 0x42800000, v202
	s_waitcnt lgkmcnt(4)
	v_mul_f32_e32 v184, 0x42800000, v204
	v_mov_b32_e32 v182, v133
	ds_read2_b32 v[214:215], v155 offset0:222 offset1:230
	ds_read2_b32 v[216:217], v154 offset0:127 offset1:135
	v_cvt_pk_fp8_f32 v182, v183, v184
	s_waitcnt lgkmcnt(3)
	v_mul_f32_e32 v190, 0x42800000, v210
	s_waitcnt lgkmcnt(2)
	v_mul_f32_e32 v192, 0x42800000, v212
	v_mov_b32_e32 v183, v133
	v_cvt_pk_fp8_f32 v183, v190, v192
	v_mul_f32_e32 v184, 0x42800000, v206
	v_mul_f32_e32 v186, 0x42800000, v208
	v_cvt_pk_fp8_f32 v182, v184, v186 op_sel:[0,0,1]
	s_waitcnt lgkmcnt(1)
	v_mul_f32_e32 v184, 0x42800000, v214
	s_waitcnt lgkmcnt(0)
	v_mul_f32_e32 v186, 0x42800000, v216
	v_cvt_pk_fp8_f32 v183, v184, v186 op_sel:[0,0,1]
	v_mul_f32_e32 v186, 0x42800000, v191
	v_mul_f32_e32 v190, 0x42800000, v193
	v_mov_b32_e32 v184, v133
	v_cvt_pk_fp8_f32 v184, v186, v190
	v_mul_f32_e32 v186, 0x42800000, v185
	v_mul_f32_e32 v190, 0x42800000, v195
	v_mul_f32_e32 v191, 0x42800000, v197
	v_mov_b32_e32 v185, v133
	v_cvt_pk_fp8_f32 v185, v190, v191
	v_mul_f32_e32 v187, 0x42800000, v187
	v_cvt_pk_fp8_f32 v184, v186, v187 op_sel:[0,0,1]
	v_mul_f32_e32 v186, 0x42800000, v199
	v_mul_f32_e32 v187, 0x42800000, v201
	v_cvt_pk_fp8_f32 v185, v186, v187 op_sel:[0,0,1]
	v_mul_f32_e32 v187, 0x42800000, v203
	v_mul_f32_e32 v190, 0x42800000, v205
	v_mov_b32_e32 v186, v133
	v_cvt_pk_fp8_f32 v186, v187, v190
	v_mul_f32_e32 v192, 0x42800000, v211
	v_mul_f32_e32 v193, 0x42800000, v213
	v_mov_b32_e32 v187, v133
	v_cvt_pk_fp8_f32 v187, v192, v193
	v_mul_f32_e32 v190, 0x42800000, v207
	v_mul_f32_e32 v191, 0x42800000, v209
	v_cvt_pk_fp8_f32 v186, v190, v191 op_sel:[0,0,1]
	v_mul_f32_e32 v190, 0x42800000, v215
	v_mul_f32_e32 v191, 0x42800000, v217
	v_cvt_pk_fp8_f32 v187, v190, v191 op_sel:[0,0,1]
	v_lshl_add_u64 v[190:191], v[188:189], 0, v[142:143]
	global_store_dwordx4 v[190:191], v[180:183], off nt
	s_nop 1
	v_lshl_add_u64 v[180:181], v[188:189], 0, v[144:145]
	global_store_dwordx4 v[180:181], v[184:187], off nt
	s_waitcnt lgkmcnt(0)
	s_cbranch_execz .LBB0_291

; __device__ __forceinline__ void t128_load(const float* W, int N, int item, int lane, f32x4 (&v)[16]) {
;     const int nblk = N / 32, kb = item / nblk, nb = item % nblk, k0 = 128 * kb, n0 = 32 * nb;
; #pragma unroll
;     for (int i = 0; i < 16; ++i) v[i] = __builtin_nontemporal_load((const f32x4*)(W + (size_t)(k0 + i * 8 + (lane >> 3)) * N + n0 + (lane & 7) * 4));
; }
; __device__ __forceinline__ int conv_stream(const Ctx& c, int j, int first, int step, const unsigned* stop, const float* w_gu, const float* w_d, unsigned char* Wgu, unsigned char* Wd) {
;     ...
;         { const int i2 = i + step; const bool more = j + CONV_SLOTS * i2 < CONV_TOTAL && !(stop && stop_poll(c, stop) >= STOP_AT);
;           cs_load(j + CONV_SLOTS * (more ? i2 : i), c.lane, w_gu, w_d, va);
;           cs_store(c, j + CONV_SLOTS * i, vb, Wgu, Wd); i = i2; if (!more) break; }
.LBB0_286:
	s_waitcnt vmcnt(4)
	v_or_b32_e32 v58, s21, v131
	v_ashrrev_i32_e32 v59, 31, v58
	v_lshlrev_b64 v[2:3], s46, v[58:59]
	v_add_u32_e32 v4, 8, v58
	v_add_u32_e32 v10, 16, v58
	v_add_u32_e32 v12, 24, v58
	v_add_u32_e32 v18, 32, v58
	v_add_u32_e32 v20, 40, v58
	v_add_u32_e32 v26, 48, v58
	v_add_u32_e32 v28, 56, v58
	v_add_u32_e32 v34, 64, v58
	v_add_u32_e32 v36, 0x48, v58
	v_add_u32_e32 v42, 0x50, v58
	v_add_u32_e32 v44, 0x58, v58
	v_add_u32_e32 v50, 0x60, v58
	v_add_u32_e32 v52, 0x68, v58
	v_add_u32_e32 v62, 0x70, v58
	v_add_u32_e32 v58, 0x78, v58
	v_ashrrev_i32_e32 v5, 31, v4
	v_ashrrev_i32_e32 v11, 31, v10
	v_ashrrev_i32_e32 v13, 31, v12
	v_ashrrev_i32_e32 v19, 31, v18
	v_ashrrev_i32_e32 v21, 31, v20
	v_ashrrev_i32_e32 v27, 31, v26
	v_ashrrev_i32_e32 v29, 31, v28
	v_ashrrev_i32_e32 v35, 31, v34
	v_ashrrev_i32_e32 v37, 31, v36
	v_ashrrev_i32_e32 v43, 31, v42
	v_ashrrev_i32_e32 v45, 31, v44
	v_ashrrev_i32_e32 v51, 31, v50
	v_ashrrev_i32_e32 v53, 31, v52
	v_ashrrev_i32_e32 v63, 31, v62
	v_ashrrev_i32_e32 v59, 31, v58
	v_lshl_add_u64 v[60:61], s[48:49], 0, v[132:133]
	v_lshlrev_b64 v[4:5], s46, v[4:5]
	v_lshlrev_b64 v[10:11], s46, v[10:11]
	v_lshlrev_b64 v[12:13], s46, v[12:13]
	v_lshlrev_b64 v[18:19], s46, v[18:19]
	v_lshlrev_b64 v[20:21], s46, v[20:21]
	v_lshlrev_b64 v[26:27], s46, v[26:27]
	v_lshlrev_b64 v[28:29], s46, v[28:29]
	v_lshlrev_b64 v[34:35], s46, v[34:35]
	v_lshlrev_b64 v[36:37], s46, v[36:37]
	v_lshlrev_b64 v[42:43], s46, v[42:43]
	v_lshlrev_b64 v[44:45], s46, v[44:45]
	v_lshlrev_b64 v[50:51], s46, v[50:51]
	v_lshlrev_b64 v[52:53], s46, v[52:53]
	v_lshlrev_b64 v[62:63], s46, v[62:63]
	v_lshlrev_b64 v[58:59], s46, v[58:59]
	v_lshl_add_u64 v[2:3], v[60:61], 0, v[2:3]
	v_lshl_add_u64 v[4:5], v[60:61], 0, v[4:5]
	v_lshl_add_u64 v[10:11], v[60:61], 0, v[10:11]
	v_lshl_add_u64 v[12:13], v[60:61], 0, v[12:13]
	v_lshl_add_u64 v[18:19], v[60:61], 0, v[18:19]
	v_lshl_add_u64 v[20:21], v[60:61], 0, v[20:21]
	v_lshl_add_u64 v[26:27], v[60:61], 0, v[26:27]
	v_lshl_add_u64 v[28:29], v[60:61], 0, v[28:29]
	v_lshl_add_u64 v[34:35], v[60:61], 0, v[34:35]
	v_lshl_add_u64 v[36:37], v[60:61], 0, v[36:37]
	v_lshl_add_u64 v[42:43], v[60:61], 0, v[42:43]
	v_lshl_add_u64 v[44:45], v[60:61], 0, v[44:45]
	v_lshl_add_u64 v[50:51], v[60:61], 0, v[50:51]
	v_lshl_add_u64 v[52:53], v[60:61], 0, v[52:53]
	v_lshl_add_u64 v[62:63], v[60:61], 0, v[62:63]
	v_lshl_add_u64 v[58:59], v[60:61], 0, v[58:59]
	s_and_b64 vcc, exec, s[44:45]
	s_cbranch_vccnz .Lcv1b_noload
	global_load_dwordx4 v[6:9], v[2:3], off nt
	s_nop 0
	global_load_dwordx4 v[2:5], v[4:5], off nt
	s_nop 0
	global_load_dwordx4 v[14:17], v[10:11], off nt
	s_nop 0
	global_load_dwordx4 v[10:13], v[12:13], off nt
	s_nop 0
	global_load_dwordx4 v[22:25], v[18:19], off nt
	s_nop 0
	global_load_dwordx4 v[18:21], v[20:21], off nt
	s_nop 0
	global_load_dwordx4 v[30:33], v[26:27], off nt
	s_nop 0
	global_load_dwordx4 v[26:29], v[28:29], off nt
	s_nop 0
	global_load_dwordx4 v[38:41], v[34:35], off nt
	s_nop 0
	global_load_dwordx4 v[34:37], v[36:37], off nt
	s_nop 0
	global_load_dwordx4 v[46:49], v[42:43], off nt
	s_nop 0
	global_load_dwordx4 v[42:45], v[44:45], off nt
	s_nop 0
	global_load_dwordx4 v[54:57], v[50:51], off nt
	s_nop 0
	global_load_dwordx4 v[50:53], v[52:53], off nt
	s_nop 0
	global_load_dwordx4 v[62:65], v[62:63], off nt
	s_nop 0
	global_load_dwordx4 v[58:61], v[58:59], off nt
.Lcv1b_noload:
	s_cmpk_gt_i32 s24, 0x7fff
	s_mov_b64 s[46:47], -1
	s_cbranch_scc0 .LBB0_288
	ds_write2_b32 v146, v70, v71 offset1:1
	ds_write2_b32 v146, v72, v73 offset0:2 offset1:3
	ds_write2_b32 v151, v66, v67 offset1:1
	ds_write2_b32 v151, v68, v69 offset0:2 offset1:3
	ds_write2_b32 v152, v78, v79 offset1:1
	ds_write2_b32 v152, v80, v81 offset0:2 offset1:3
	ds_write2_b32 v153, v74, v75 offset1:1
	ds_write2_b32 v153, v76, v77 offset0:2 offset1:3
	ds_write2_b32 v156, v86, v87 offset1:1
	ds_write2_b32 v157, v88, v89 offset1:1
	ds_write2_b32 v158, v82, v83 offset1:1
	ds_write2_b32 v159, v84, v85 offset1:1
	ds_write2_b32 v160, v94, v95 offset1:1
	ds_write2_b32 v161, v96, v97 offset1:1
	ds_write2_b32 v162, v90, v91 offset1:1
	ds_write2_b32 v163, v92, v93 offset1:1
	ds_write2_b32 v164, v102, v103 offset1:1
	ds_write2_b32 v165, v104, v105 offset1:1
	ds_write2_b32 v166, v98, v99 offset1:1
	ds_write2_b32 v167, v100, v101 offset1:1
	ds_write2_b32 v168, v110, v111 offset1:1
	ds_write2_b32 v169, v112, v113 offset1:1
	ds_write2_b32 v170, v106, v107 offset1:1
	ds_write2_b32 v171, v108, v109 offset1:1
	ds_write2_b32 v172, v118, v119 offset1:1
	ds_write2_b32 v173, v120, v121 offset1:1
	ds_write2_b32 v174, v114, v115 offset1:1
	ds_write2_b32 v175, v116, v117 offset1:1
	ds_write2_b32 v176, v126, v127 offset1:1
	ds_write2_b32 v177, v128, v129 offset1:1
	ds_write2_b32 v178, v122, v123 offset1:1
	ds_write2_b32 v179, v124, v125 offset1:1
	s_waitcnt lgkmcnt(0)
	ds_read2_b32 v[184:185], v150 offset1:8
	ds_read2_b32 v[186:187], v150 offset0:33 offset1:41
	ds_read2_b32 v[190:191], v150 offset0:66 offset1:74
	ds_read2_b32 v[192:193], v150 offset0:99 offset1:107
	v_mov_b32_e32 v180, v133
	ds_read2_b32 v[194:195], v150 offset0:132 offset1:140
	ds_read2_b32 v[196:197], v150 offset0:165 offset1:173
	s_waitcnt lgkmcnt(5)
	v_mul_f32_e32 v132, 0x42800000, v184
	s_waitcnt lgkmcnt(4)
	v_mul_f32_e32 v181, 0x42800000, v186
	v_cvt_pk_fp8_f32 v180, v132, v181
	s_waitcnt lgkmcnt(3)
	v_mul_f32_e32 v132, 0x42800000, v190
	s_waitcnt lgkmcnt(2)
	v_mul_f32_e32 v181, 0x42800000, v192
	ds_read2_b32 v[198:199], v150 offset0:198 offset1:206
	ds_read2_b32 v[200:201], v150 offset0:231 offset1:239
	v_cvt_pk_fp8_f32 v180, v132, v181 op_sel:[0,0,1]
	s_waitcnt lgkmcnt(3)
; #define LAS __attribute__((address_space(3)))
; #define LDS_WAIT() asm volatile("s_waitcnt lgkmcnt(0)" ::: "memory")
; template <int MODE>
; __device__ __forceinline__ void t128_store(const Ctx& c, const f32x4 (&v)[16], int K, int N, unsigned char* WT, int item) {
;     LAS float* scr = (LAS float*)(c.lds + c.wave * CONV_SCR);
;     const int nblk = N / 32, kb = item / nblk, nb = item % nblk, k0 = 128 * kb, n0 = 32 * nb, lane = c.lane;
; #pragma unroll
;     for (int i = 0; i < 16; ++i) { LAS float* d = scr + (i * 8 + (lane >> 3)) * 33 + (lane & 7) * 4; d[0] = v[i].x; d[1] = v[i].y; d[2] = v[i].z; d[3] = v[i].w; }
;     LDS_WAIT(); asm volatile("" ::: "memory");
;     const int cc = lane & 7;
; #pragma unroll
;     for (int j = 0; j < 4; ++j) { const int n = (lane >> 3) + 8 * j; const LAS float* s = scr + (16 * cc) * 33 + n; int w[4];
; #pragma unroll
;         for (int q = 0; q < 4; ++q) { int t = 0; t = __builtin_amdgcn_cvt_pk_fp8_f32(s[(4 * q) * 33] * WSCALE, s[(4 * q + 1) * 33] * WSCALE, t, false);
;             t = __builtin_amdgcn_cvt_pk_fp8_f32(s[(4 * q + 2) * 33] * WSCALE, s[(4 * q + 3) * 33] * WSCALE, t, true); w[q] = t; }
;         const int dr = drow_of<MODE>(n0 + n);
;         __builtin_nontemporal_store((u32x4){(unsigned)w[0], (unsigned)w[1], (unsigned)w[2], (unsigned)w[3]}, (u32x4*)(WT + (size_t)dr * K + k0 + 16 * cc)); }
;     LDS_WAIT(); asm volatile("" ::: "memory");
; }
; __device__ __forceinline__ void cs_store(const Ctx& c, int it, const f32x4 (&v)[16], unsigned char* Wgu, unsigned char* Wd) {
;     if (it < I_D) { constexpr int per = (DFF / 128) * (D / 32); t128_store<0>(c, v, DFF, D, Wd + (size_t)(it / per) * D * DFF, it % per); }
;     else { const int r = it - I_D; constexpr int per = (D / 128) * (4096 / 32); t128_store<1>(c, v, D, 4096, Wgu + (size_t)(r / per) * 4096 * D, r % per); }
	v_mul_f32_e32 v132, 0x42800000, v194
	s_waitcnt lgkmcnt(2)
	v_mul_f32_e32 v182, 0x42800000, v196
	v_mov_b32_e32 v181, v133
	ds_read2_b32 v[202:203], v155 offset0:8 offset1:16
	ds_read2_b32 v[204:205], v155 offset0:41 offset1:49
	v_cvt_pk_fp8_f32 v181, v132, v182
	ds_read2_b32 v[206:207], v155 offset0:74 offset1:82
	ds_read2_b32 v[208:209], v155 offset0:107 offset1:115
	ds_read2_b32 v[210:211], v155 offset0:140 offset1:148
	ds_read2_b32 v[212:213], v155 offset0:173 offset1:181
	s_waitcnt lgkmcnt(7)
	v_mul_f32_e32 v132, 0x42800000, v198
	s_waitcnt lgkmcnt(6)
	v_mul_f32_e32 v182, 0x42800000, v200
	v_cvt_pk_fp8_f32 v181, v132, v182 op_sel:[0,0,1]
	s_waitcnt lgkmcnt(5)
	v_mul_f32_e32 v132, 0x42800000, v202
	s_waitcnt lgkmcnt(4)
	v_mul_f32_e32 v183, 0x42800000, v204
	v_mov_b32_e32 v182, v133
	ds_read2_b32 v[214:215], v155 offset0:206 offset1:214
	ds_read2_b32 v[216:217], v155 offset0:239 offset1:247
	v_cvt_pk_fp8_f32 v182, v132, v183
	s_waitcnt lgkmcnt(3)
	v_mul_f32_e32 v186, 0x42800000, v210
	s_waitcnt lgkmcnt(2)
	v_mul_f32_e32 v190, 0x42800000, v212
	v_mov_b32_e32 v183, v133
	v_cvt_pk_fp8_f32 v183, v186, v190
	v_mul_f32_e32 v132, 0x42800000, v206
	v_mul_f32_e32 v184, 0x42800000, v208
	v_cvt_pk_fp8_f32 v182, v132, v184 op_sel:[0,0,1]
	s_waitcnt lgkmcnt(1)
	v_mul_f32_e32 v132, 0x42800000, v214
	s_waitcnt lgkmcnt(0)
	v_mul_f32_e32 v184, 0x42800000, v216
	v_cvt_pk_fp8_f32 v183, v132, v184 op_sel:[0,0,1]
	v_mul_f32_e32 v132, 0x42800000, v185
	v_mul_f32_e32 v185, 0x42800000, v187
	v_mov_b32_e32 v184, v133
	v_cvt_pk_fp8_f32 v184, v132, v185
	v_mul_f32_e32 v187, 0x42800000, v195
	v_mul_f32_e32 v190, 0x42800000, v197
	v_mov_b32_e32 v185, v133
	v_cvt_pk_fp8_f32 v185, v187, v190
	v_mul_f32_e32 v132, 0x42800000, v191
	v_mul_f32_e32 v186, 0x42800000, v193
	v_cvt_pk_fp8_f32 v184, v132, v186 op_sel:[0,0,1]
	v_mul_f32_e32 v132, 0x42800000, v199
	v_mul_f32_e32 v186, 0x42800000, v201
	s_add_i32 s20, s19, 0xffff7c00
	v_cvt_pk_fp8_f32 v185, v132, v186 op_sel:[0,0,1]
	v_mul_f32_e32 v132, 0x42800000, v203
	v_mul_f32_e32 v187, 0x42800000, v205
	v_mov_b32_e32 v186, v133
	s_lshr_b32 s42, s20, 11
	v_cvt_pk_fp8_f32 v186, v132, v187
	v_mul_f32_e32 v191, 0x42800000, v211
	v_mul_f32_e32 v192, 0x42800000, v213
	v_mov_b32_e32 v187, v133
	s_lshl_b64 s[20:21], s[42:43], 23
	v_cvt_pk_fp8_f32 v187, v191, v192
	s_add_u32 s20, s38, s20
	s_addc_u32 s21, s39, s21
	s_and_b32 s25, s24, 0x780
	v_mul_f32_e32 v132, 0x42800000, v207
	v_mul_f32_e32 v190, 0x42800000, v209
	s_add_u32 s20, s20, s25
	v_cvt_pk_fp8_f32 v186, v132, v190 op_sel:[0,0,1]
	v_mul_f32_e32 v132, 0x42800000, v215
	v_mul_f32_e32 v190, 0x42800000, v217
	s_addc_u32 s21, s21, 0
	v_cvt_pk_fp8_f32 v187, v132, v190 op_sel:[0,0,1]
	v_lshl_add_u64 v[188:189], s[20:21], 0, v[134:135]
	ds_read2_b32 v[190:191], v150 offset0:16 offset1:24
	ds_read2_b32 v[192:193], v150 offset0:49 offset1:57
	v_lshl_add_u64 v[218:219], v[188:189], 0, v[138:139]
	global_store_dwordx4 v[218:219], v[180:183], off nt
	s_mov_b64 s[46:47], 0
	s_waitcnt lgkmcnt(1)
	v_mul_f32_e32 v132, 0x42800000, v190
	v_lshl_add_u64 v[180:181], v[188:189], 0, v[140:141]
	global_store_dwordx4 v[180:181], v[184:187], off nt
	ds_read2_b32 v[184:185], v150 offset0:82 offset1:90
	ds_read2_b32 v[186:187], v150 offset0:115 offset1:123
	s_waitcnt lgkmcnt(2)
	v_mul_f32_e32 v181, 0x42800000, v192
	v_mov_b32_e32 v180, v133
	ds_read2_b32 v[194:195], v150 offset0:148 offset1:156
	ds_read2_b32 v[196:197], v150 offset0:181 offset1:189
	v_cvt_pk_fp8_f32 v180, v132, v181
	s_waitcnt lgkmcnt(3)
	v_mul_f32_e32 v132, 0x42800000, v184
	s_waitcnt lgkmcnt(2)
	v_mul_f32_e32 v181, 0x42800000, v186
	ds_read2_b32 v[198:199], v150 offset0:214 offset1:222
	ds_read2_b32 v[200:201], v150 offset0:247 offset1:255
	v_cvt_pk_fp8_f32 v180, v132, v181 op_sel:[0,0,1]
	s_waitcnt lgkmcnt(3)
	v_mul_f32_e32 v132, 0x42800000, v194
	s_waitcnt lgkmcnt(2)
	v_mul_f32_e32 v182, 0x42800000, v196
	v_mov_b32_e32 v181, v133
	ds_read2_b32 v[202:203], v155 offset0:24 offset1:32
	ds_read2_b32 v[204:205], v155 offset0:57 offset1:65
	v_cvt_pk_fp8_f32 v181, v132, v182
	ds_read2_b32 v[206:207], v155 offset0:90 offset1:98
	ds_read2_b32 v[208:209], v155 offset0:123 offset1:131
	ds_read2_b32 v[210:211], v155 offset0:156 offset1:164
	ds_read2_b32 v[212:213], v155 offset0:189 offset1:197
	s_waitcnt lgkmcnt(7)
	v_mul_f32_e32 v132, 0x42800000, v198
	s_waitcnt lgkmcnt(6)
	v_mul_f32_e32 v182, 0x42800000, v200
	v_cvt_pk_fp8_f32 v181, v132, v182 op_sel:[0,0,1]
	s_waitcnt lgkmcnt(5)
	v_mul_f32_e32 v132, 0x42800000, v202
	s_waitcnt lgkmcnt(4)
	v_mul_f32_e32 v183, 0x42800000, v204
	v_mov_b32_e32 v182, v133
	ds_read2_b32 v[214:215], v155 offset0:222 offset1:230
	ds_read2_b32 v[216:217], v154 offset0:127 offset1:135
	v_cvt_pk_fp8_f32 v182, v132, v183
	s_waitcnt lgkmcnt(3)
	v_mul_f32_e32 v186, 0x42800000, v210
	s_waitcnt lgkmcnt(2)
	v_mul_f32_e32 v190, 0x42800000, v212
	v_mov_b32_e32 v183, v133
	v_cvt_pk_fp8_f32 v183, v186, v190
	v_mul_f32_e32 v132, 0x42800000, v206
	v_mul_f32_e32 v184, 0x42800000, v208
	v_cvt_pk_fp8_f32 v182, v132, v184 op_sel:[0,0,1]
	s_waitcnt lgkmcnt(1)
	v_mul_f32_e32 v132, 0x42800000, v214
	s_waitcnt lgkmcnt(0)
	v_mul_f32_e32 v184, 0x42800000, v216
	v_cvt_pk_fp8_f32 v183, v132, v184 op_sel:[0,0,1]
	v_mul_f32_e32 v132, 0x42800000, v191
	v_mul_f32_e32 v186, 0x42800000, v193
	v_mov_b32_e32 v184, v133
	v_cvt_pk_fp8_f32 v184, v132, v186
	v_mul_f32_e32 v132, 0x42800000, v185
	v_mul_f32_e32 v186, 0x42800000, v187
	v_mul_f32_e32 v187, 0x42800000, v195
	v_mul_f32_e32 v190, 0x42800000, v197
	v_mov_b32_e32 v185, v133
	v_cvt_pk_fp8_f32 v185, v187, v190
	v_cvt_pk_fp8_f32 v184, v132, v186 op_sel:[0,0,1]
	v_mul_f32_e32 v132, 0x42800000, v199
	v_mul_f32_e32 v186, 0x42800000, v201
	v_cvt_pk_fp8_f32 v185, v132, v186 op_sel:[0,0,1]
	v_mul_f32_e32 v132, 0x42800000, v203
	v_mul_f32_e32 v187, 0x42800000, v205
	v_mov_b32_e32 v186, v133
	v_cvt_pk_fp8_f32 v186, v132, v187
	v_mul_f32_e32 v191, 0x42800000, v211
	v_mul_f32_e32 v192, 0x42800000, v213
	v_mov_b32_e32 v187, v133
	v_cvt_pk_fp8_f32 v187, v191, v192
	v_mul_f32_e32 v132, 0x42800000, v207
	v_mul_f32_e32 v190, 0x42800000, v209
	v_cvt_pk_fp8_f32 v186, v132, v190 op_sel:[0,0,1]
	v_mul_f32_e32 v132, 0x42800000, v215
	v_mul_f32_e32 v190, 0x42800000, v217
	v_cvt_pk_fp8_f32 v187, v132, v190 op_sel:[0,0,1]
	v_lshl_add_u64 v[190:191], v[188:189], 0, v[142:143]
	global_store_dwordx4 v[190:191], v[180:183], off nt
	s_nop 1
	v_lshl_add_u64 v[180:181], v[188:189], 0, v[144:145]
	global_store_dwordx4 v[180:181], v[184:187], off nt
	s_waitcnt lgkmcnt(0)
